# baseline (speedup 1.0000x reference)
_Z13prep_w_kernelPKfS0_S0_PDv8_DF16_:
	s_load_dword s3, s[0:1], 0x2c
	s_waitcnt lgkmcnt(0)
	s_and_b32 s3, s3, 0xffff
	s_mul_i32 s2, s2, s3
	v_add_u32_e32 v0, s2, v0
	s_movk_i32 s2, 0x6000
	v_cmp_gt_i32_e32 vcc, s2, v0
	s_and_saveexec_b64 s[2:3], vcc
	s_cbranch_execz .LBB0_2
	s_load_dwordx8 s[4:11], s[0:1], 0x0
	v_ashrrev_i32_e32 v1, 6, v0
	s_mov_b32 s0, 0x55555556
	v_mul_hi_i32 v2, v1, s0
	v_lshrrev_b32_e32 v3, 31, v2
	v_add_u32_e32 v4, v2, v3
	v_lshl_add_u32 v2, v4, 1, v4
	s_mov_b32 s0, 0x2aaaaaab
	v_sub_u32_e32 v2, v1, v2
	v_mul_hi_i32 v1, v1, s0
	v_lshrrev_b32_e32 v3, 31, v1
	v_lshrrev_b32_e32 v1, 4, v1
	v_add_u32_e32 v1, v1, v3
	s_waitcnt lgkmcnt(0)
	v_mov_b32_e32 v3, s8
	v_mov_b32_e32 v5, s6
	v_cmp_eq_u32_e32 vcc, 1, v2
	v_mov_b32_e32 v6, s7
	v_lshlrev_b32_e32 v4, 5, v4
	v_cndmask_b32_e32 v5, v3, v5, vcc
	v_mov_b32_e32 v3, s9
	v_cndmask_b32_e32 v3, v3, v6, vcc
	v_cmp_eq_u32_e32 vcc, 0, v2
	v_mov_b32_e32 v2, s5
	v_and_b32_e32 v4, 0x3e0, v4
	v_cndmask_b32_e32 v3, v3, v2, vcc
	v_mov_b32_e32 v2, s4
	v_cndmask_b32_e32 v2, v5, v2, vcc
	v_lshrrev_b32_e32 v5, 1, v0
	v_and_or_b32 v5, v5, 24, v4
	v_and_b32_e32 v4, 15, v0
	v_lshl_or_b32 v4, v1, 4, v4
	v_lshlrev_b32_e32 v8, 6, v5
	v_add_u32_e32 v10, v4, v8
	v_ashrrev_i32_e32 v11, 31, v10
	v_ashrrev_i32_e32 v5, 31, v4
	v_mov_b32_e32 v9, 0
	v_mov_b32_e32 v6, 0x42800000
	v_mov_b32_e32 v7, 0x4138aa3b
	v_lshl_add_u64 v[10:11], v[10:11], 2, v[2:3]
	v_lshl_add_u64 v[4:5], v[4:5], 0, v[8:9]
	v_cndmask_b32_e32 v6, v6, v7, vcc
	v_lshl_add_u64 v[2:3], v[4:5], 2, v[2:3]
	global_load_dword v7, v[10:11], off
	global_load_dword v4, v[2:3], off offset:256
	global_load_dword v5, v[2:3], off offset:512
	global_load_dword v8, v[2:3], off offset:768
	global_load_dword v9, v[2:3], off offset:1024
	global_load_dword v12, v[2:3], off offset:1280
	global_load_dword v13, v[2:3], off offset:1536
	global_load_dword v14, v[2:3], off offset:1792
	v_ashrrev_i32_e32 v1, 31, v0
	v_lshl_add_u64 v[0:1], v[0:1], 4, s[10:11]
	s_waitcnt vmcnt(7)
	v_fma_mixlo_f16 v7, v6, v7, 0
	s_waitcnt vmcnt(5)
	v_pk_mul_f32 v[2:3], v[6:7], v[4:5] op_sel_hi:[0,1]
	v_cvt_pk_f16_f32 v3, v2, v3
	s_waitcnt vmcnt(3)
	v_pk_mul_f32 v[4:5], v[6:7], v[8:9] op_sel_hi:[0,1]
	v_cvt_pk_f16_f32 v4, v4, v5
	s_waitcnt vmcnt(1)
	v_pk_mul_f32 v[8:9], v[6:7], v[12:13] op_sel_hi:[0,1]
	v_cvt_pk_f16_f32 v5, v8, v9
	v_pack_b32_f16 v2, v7, v3
	v_alignbit_b32 v3, v4, v3, 16
	v_alignbit_b32 v4, v5, v4, 16
	v_lshrrev_b32_e32 v5, 16, v5
	s_waitcnt vmcnt(0)
	v_fma_mixhi_f16 v5, v6, v14, 0
	global_store_dwordx4 v[0:1], v[2:5], off sc1

.LBB1_3:
	s_load_dwordx8 s[4:11], s[0:1], 0x8
	s_lshr_b32 s16, s13, 6
	s_mul_i32 s14, s16, 0x1800
	s_mov_b32 s15, 0
	s_lshl_b64 s[18:19], s[14:15], 4
	v_and_b32_e32 v2, 63, v0
	s_waitcnt lgkmcnt(0)
	s_add_u32 s4, s4, s18
	s_addc_u32 s5, s5, s19
	v_lshlrev_b32_e32 v54, 4, v2
	v_mov_b32_e32 v55, 0
	v_lshl_add_u64 v[18:19], s[4:5], 0, v[54:55]
	s_bfe_u32 s4, s2, 0x40003
	s_mul_i32 s14, s4, 0x1800
	v_lshl_add_u64 v[20:21], v[18:19], 0, s[14:15]
	global_load_dwordx4 v[2:5], v[20:21], off offset:2048
	global_load_dwordx4 v[6:9], v[20:21], off
	global_load_dwordx4 v[10:13], v[20:21], off offset:1024
	v_lshrrev_b32_e32 v14, 1, v0
	v_bfe_u32 v56, v0, 4, 2
	v_lshlrev_b32_e32 v54, 7, v1
	v_bitop3_b32 v14, v56, v14, 7 bitop3:0x78
	v_lshl_or_b32 v57, v14, 4, v54
	global_load_dwordx4 v[14:17], v[20:21], off offset:3072
	s_movk_i32 s2, 0x1000
	s_add_i32 s5, s3, 1
	s_and_b32 s5, s5, 15
	v_add_co_u32_e32 v44, vcc, s2, v20
	s_mul_i32 s14, s5, 0x1800
	s_nop 0
	v_addc_co_u32_e32 v45, vcc, 0, v21, vcc
	v_lshl_add_u64 v[46:47], v[18:19], 0, s[14:15]
	global_load_dwordx4 v[20:23], v[44:45], off
	global_load_dwordx4 v[24:27], v[44:45], off offset:1024
	global_load_dwordx4 v[28:31], v[46:47], off
	global_load_dwordx4 v[32:35], v[46:47], off offset:1024
	global_load_dwordx4 v[36:39], v[46:47], off offset:2048
	global_load_dwordx4 v[40:43], v[46:47], off offset:3072
	s_add_i32 s13, s3, 2
	s_and_b32 s13, s13, 15
	v_add_co_u32_e32 v52, vcc, s2, v46
	s_mul_i32 s14, s13, 0x1800
	s_nop 0
	v_addc_co_u32_e32 v53, vcc, 0, v47, vcc
	v_lshl_add_u64 v[58:59], v[18:19], 0, s[14:15]
	global_load_dwordx4 v[44:47], v[52:53], off
	global_load_dwordx4 v[48:51], v[52:53], off offset:1024
	global_load_dwordx4 v[60:63], v[58:59], off
	global_load_dwordx4 v[64:67], v[58:59], off offset:1024
	global_load_dwordx4 v[68:71], v[58:59], off offset:2048
	global_load_dwordx4 v[72:75], v[58:59], off offset:3072
	v_add_co_u32_e32 v52, vcc, s2, v58
	s_add_i32 s5, s3, 3
	s_nop 0
	v_addc_co_u32_e32 v53, vcc, 0, v59, vcc
	global_load_dwordx4 v[76:79], v[52:53], off
	global_load_dwordx4 v[80:83], v[52:53], off offset:1024
	s_barrier
	ds_read_b128 v[84:87], v57
	ds_read_b128 v[88:91], v57 offset:2048
	ds_read_b128 v[96:99], v57 offset:4096
	ds_read_b128 v[104:107], v57 offset:6144
	v_bfe_u32 v52, v0, 1, 3
	v_bitop3_b32 v52, v56, v52, 4 bitop3:0x36
	v_lshl_or_b32 v58, v52, 4, v54
	ds_read_b128 v[124:127], v58
	ds_read_b128 v[128:131], v58 offset:4096
	ds_read_b128 v[132:135], v58 offset:6144
	s_and_b32 s5, s5, 15
	s_mul_i32 s14, s5, 0x1800
	v_lshl_add_u64 v[52:53], v[18:19], 0, s[14:15]
	s_add_i32 s5, s3, 4
	s_and_b32 s5, s5, 15
	s_mul_i32 s14, s5, 0x1800
	s_add_i32 s5, s3, 5
	s_and_b32 s5, s5, 15
	s_xor_b32 s4, s4, 8
	v_or_b32_e32 v59, 0x1a000, v57
	s_ashr_i32 s13, s12, 31
	v_lshl_or_b32 v54, s16, 11, v54
	v_or_b32_e32 v156, s12, v1
	v_ashrrev_i32_e32 v157, 31, v156
	s_waitcnt vmcnt(17) lgkmcnt(6)
	v_mfma_f32_16x16x32_f16 v[92:95], v[84:87], v[2:5], 0
	s_waitcnt lgkmcnt(5)
	v_mfma_f32_16x16x32_f16 v[100:103], v[88:91], v[2:5], 0
	s_waitcnt lgkmcnt(4)
	v_mfma_f32_16x16x32_f16 v[108:111], v[96:99], v[2:5], 0
	s_waitcnt lgkmcnt(3)
	v_mfma_f32_16x16x32_f16 v[2:5], v[104:107], v[2:5], 0
	s_waitcnt vmcnt(16)
	v_mfma_f32_16x16x32_f16 v[112:115], v[6:9], v[84:87], 0
	s_waitcnt vmcnt(15)
	v_mfma_f32_16x16x32_f16 v[84:87], v[10:13], v[84:87], 0
	v_mfma_f32_16x16x32_f16 v[116:119], v[6:9], v[88:91], 0
	v_mfma_f32_16x16x32_f16 v[88:91], v[10:13], v[88:91], 0
	v_mfma_f32_16x16x32_f16 v[120:123], v[6:9], v[96:99], 0
	v_mfma_f32_16x16x32_f16 v[96:99], v[10:13], v[96:99], 0
	v_mfma_f32_16x16x32_f16 v[6:9], v[6:9], v[104:107], 0
	v_mfma_f32_16x16x32_f16 v[10:13], v[10:13], v[104:107], 0
	ds_read_b128 v[104:107], v58 offset:2048
	s_waitcnt vmcnt(12) lgkmcnt(3)
	v_mfma_f32_16x16x32_f16 v[92:95], v[124:127], v[24:27], v[92:95]
	s_waitcnt lgkmcnt(0)
	v_mfma_f32_16x16x32_f16 v[100:103], v[104:107], v[24:27], v[100:103]
	v_mfma_f32_16x16x32_f16 v[108:111], v[128:131], v[24:27], v[108:111]
	v_mfma_f32_16x16x32_f16 v[2:5], v[132:135], v[24:27], v[2:5]
	v_mfma_f32_16x16x32_f16 v[24:27], v[14:17], v[124:127], v[112:115]
	v_mfma_f32_16x16x32_f16 v[84:87], v[20:23], v[124:127], v[84:87]
	v_mfma_f32_16x16x32_f16 v[112:115], v[14:17], v[104:107], v[116:119]
	v_mfma_f32_16x16x32_f16 v[88:91], v[20:23], v[104:107], v[88:91]
	v_mfma_f32_16x16x32_f16 v[104:107], v[14:17], v[128:131], v[120:123]
	v_mfma_f32_16x16x32_f16 v[96:99], v[20:23], v[128:131], v[96:99]
	v_mfma_f32_16x16x32_f16 v[6:9], v[14:17], v[132:135], v[6:9]
	v_mfma_f32_16x16x32_f16 v[10:13], v[20:23], v[132:135], v[10:13]
	global_load_dwordx4 v[14:17], v[52:53], off
	global_load_dwordx4 v[20:23], v[52:53], off offset:1024
	global_load_dwordx4 v[116:119], v[52:53], off offset:2048
	global_load_dwordx4 v[120:123], v[52:53], off offset:3072
	v_add_co_u32_e32 v52, vcc, s2, v52
	s_nop 1
	v_addc_co_u32_e32 v53, vcc, 0, v53, vcc
	global_load_dwordx4 v[124:127], v[52:53], off
	global_load_dwordx4 v[128:131], v[52:53], off offset:1024
	s_barrier
	ds_read_b128 v[132:135], v57 offset:8192
	ds_read_b128 v[136:139], v57 offset:10240
	s_waitcnt vmcnt(17) lgkmcnt(1)
	v_mfma_f32_16x16x32_f16 v[24:27], v[28:31], v[132:135], v[24:27]
	v_lshl_add_u64 v[52:53], v[18:19], 0, s[14:15]
	s_mul_i32 s14, s5, 0x1800
	s_add_i32 s5, s3, 6
	s_waitcnt vmcnt(16)
	v_mfma_f32_16x16x32_f16 v[84:87], v[32:35], v[132:135], v[84:87]
	s_and_b32 s5, s5, 15
	s_waitcnt vmcnt(15)
	v_mfma_f32_16x16x32_f16 v[92:95], v[132:135], v[36:39], v[92:95]
	s_waitcnt lgkmcnt(0)
	v_mfma_f32_16x16x32_f16 v[112:115], v[28:31], v[136:139], v[112:115]
	v_mfma_f32_16x16x32_f16 v[88:91], v[32:35], v[136:139], v[88:91]
	v_mfma_f32_16x16x32_f16 v[100:103], v[136:139], v[36:39], v[100:103]
	ds_read_b128 v[132:135], v57 offset:12288
	ds_read_b128 v[136:139], v57 offset:14336
	s_waitcnt lgkmcnt(1)
	v_mfma_f32_16x16x32_f16 v[104:107], v[28:31], v[132:135], v[104:107]
	v_mfma_f32_16x16x32_f16 v[96:99], v[32:35], v[132:135], v[96:99]
	s_waitcnt lgkmcnt(0)
	v_mfma_f32_16x16x32_f16 v[6:9], v[28:31], v[136:139], v[6:9]
	v_mfma_f32_16x16x32_f16 v[10:13], v[32:35], v[136:139], v[10:13]
	ds_read_b128 v[28:31], v58 offset:8192
	ds_read_b128 v[32:35], v58 offset:10240
	v_mfma_f32_16x16x32_f16 v[108:111], v[132:135], v[36:39], v[108:111]
	v_mfma_f32_16x16x32_f16 v[2:5], v[136:139], v[36:39], v[2:5]
	s_waitcnt vmcnt(14) lgkmcnt(1)
	v_mfma_f32_16x16x32_f16 v[24:27], v[40:43], v[28:31], v[24:27]
	s_waitcnt vmcnt(13)
	v_mfma_f32_16x16x32_f16 v[36:39], v[44:47], v[28:31], v[84:87]
	s_waitcnt vmcnt(12)
	v_mfma_f32_16x16x32_f16 v[28:31], v[28:31], v[48:51], v[92:95]
	s_waitcnt lgkmcnt(0)
	v_mfma_f32_16x16x32_f16 v[84:87], v[40:43], v[32:35], v[112:115]
	v_mfma_f32_16x16x32_f16 v[88:91], v[44:47], v[32:35], v[88:91]
	v_mfma_f32_16x16x32_f16 v[32:35], v[32:35], v[48:51], v[100:103]
	ds_read_b128 v[92:95], v58 offset:12288
	s_nop 1
	ds_read_b128 v[100:103], v58 offset:14336
	s_waitcnt lgkmcnt(1)
	v_mfma_f32_16x16x32_f16 v[104:107], v[40:43], v[92:95], v[104:107]
	v_mfma_f32_16x16x32_f16 v[96:99], v[44:47], v[92:95], v[96:99]
	v_mfma_f32_16x16x32_f16 v[92:95], v[92:95], v[48:51], v[108:111]
	s_waitcnt lgkmcnt(0)
	v_mfma_f32_16x16x32_f16 v[6:9], v[40:43], v[100:103], v[6:9]
	v_mfma_f32_16x16x32_f16 v[10:13], v[44:47], v[100:103], v[10:13]
	v_mfma_f32_16x16x32_f16 v[2:5], v[100:103], v[48:51], v[2:5]
	global_load_dwordx4 v[40:43], v[52:53], off
	global_load_dwordx4 v[44:47], v[52:53], off offset:1024
	global_load_dwordx4 v[48:51], v[52:53], off offset:2048
	global_load_dwordx4 v[100:103], v[52:53], off offset:3072
	v_add_co_u32_e32 v52, vcc, s2, v52
	s_nop 1
	v_addc_co_u32_e32 v53, vcc, 0, v53, vcc
	global_load_dwordx4 v[108:111], v[52:53], off
	global_load_dwordx4 v[112:115], v[52:53], off offset:1024
	s_barrier
	ds_read_b128 v[132:135], v57 offset:16384
	ds_read_b128 v[136:139], v57 offset:18432
	s_waitcnt vmcnt(17) lgkmcnt(1)
	v_mfma_f32_16x16x32_f16 v[24:27], v[60:63], v[132:135], v[24:27]
	v_lshl_add_u64 v[52:53], v[18:19], 0, s[14:15]
	s_mul_i32 s14, s5, 0x1800
	s_add_i32 s5, s3, 7
	s_waitcnt vmcnt(16)
	v_mfma_f32_16x16x32_f16 v[36:39], v[64:67], v[132:135], v[36:39]
	s_and_b32 s5, s5, 15
	s_waitcnt vmcnt(15)
	v_mfma_f32_16x16x32_f16 v[28:31], v[132:135], v[68:71], v[28:31]
	s_waitcnt lgkmcnt(0)
	v_mfma_f32_16x16x32_f16 v[84:87], v[60:63], v[136:139], v[84:87]
	v_mfma_f32_16x16x32_f16 v[88:91], v[64:67], v[136:139], v[88:91]
	v_mfma_f32_16x16x32_f16 v[32:35], v[136:139], v[68:71], v[32:35]
	ds_read_b128 v[132:135], v57 offset:20480
	ds_read_b128 v[136:139], v57 offset:22528
	s_waitcnt lgkmcnt(1)
	v_mfma_f32_16x16x32_f16 v[104:107], v[60:63], v[132:135], v[104:107]
	v_mfma_f32_16x16x32_f16 v[96:99], v[64:67], v[132:135], v[96:99]
	s_waitcnt lgkmcnt(0)
	v_mfma_f32_16x16x32_f16 v[6:9], v[60:63], v[136:139], v[6:9]
	v_mfma_f32_16x16x32_f16 v[10:13], v[64:67], v[136:139], v[10:13]
	ds_read_b128 v[60:63], v58 offset:16384
	ds_read_b128 v[64:67], v58 offset:18432
	v_mfma_f32_16x16x32_f16 v[92:95], v[132:135], v[68:71], v[92:95]
	v_mfma_f32_16x16x32_f16 v[2:5], v[136:139], v[68:71], v[2:5]
	s_waitcnt vmcnt(14) lgkmcnt(1)
	v_mfma_f32_16x16x32_f16 v[24:27], v[72:75], v[60:63], v[24:27]
	s_waitcnt vmcnt(13)
	v_mfma_f32_16x16x32_f16 v[36:39], v[76:79], v[60:63], v[36:39]
	s_waitcnt vmcnt(12)
	v_mfma_f32_16x16x32_f16 v[28:31], v[60:63], v[80:83], v[28:31]
	s_waitcnt lgkmcnt(0)
	v_mfma_f32_16x16x32_f16 v[60:63], v[72:75], v[64:67], v[84:87]
	v_mfma_f32_16x16x32_f16 v[68:71], v[76:79], v[64:67], v[88:91]
	v_mfma_f32_16x16x32_f16 v[32:35], v[64:67], v[80:83], v[32:35]
	ds_read_b128 v[64:67], v58 offset:20480
	ds_read_b128 v[84:87], v58 offset:22528
	s_waitcnt lgkmcnt(1)
	v_mfma_f32_16x16x32_f16 v[88:91], v[72:75], v[64:67], v[104:107]
	v_mfma_f32_16x16x32_f16 v[96:99], v[76:79], v[64:67], v[96:99]
	v_mfma_f32_16x16x32_f16 v[64:67], v[64:67], v[80:83], v[92:95]
	s_waitcnt lgkmcnt(0)
	v_mfma_f32_16x16x32_f16 v[6:9], v[72:75], v[84:87], v[6:9]
	v_mfma_f32_16x16x32_f16 v[10:13], v[76:79], v[84:87], v[10:13]
	v_mfma_f32_16x16x32_f16 v[2:5], v[84:87], v[80:83], v[2:5]
	global_load_dwordx4 v[72:75], v[52:53], off
	global_load_dwordx4 v[76:79], v[52:53], off offset:1024
	global_load_dwordx4 v[80:83], v[52:53], off offset:2048
	global_load_dwordx4 v[84:87], v[52:53], off offset:3072
	v_add_co_u32_e32 v52, vcc, s2, v52
	s_nop 1
	v_addc_co_u32_e32 v53, vcc, 0, v53, vcc
	global_load_dwordx4 v[92:95], v[52:53], off
	global_load_dwordx4 v[104:107], v[52:53], off offset:1024
	s_barrier
	ds_read_b128 v[132:135], v57 offset:24576
	ds_read_b128 v[136:139], v57 offset:26624
	s_waitcnt vmcnt(17) lgkmcnt(1)
	v_mfma_f32_16x16x32_f16 v[24:27], v[14:17], v[132:135], v[24:27]
	v_lshl_add_u64 v[52:53], v[18:19], 0, s[14:15]
	s_mul_i32 s14, s5, 0x1800
	s_waitcnt vmcnt(16)
	v_mfma_f32_16x16x32_f16 v[36:39], v[20:23], v[132:135], v[36:39]
	s_waitcnt vmcnt(15)
	v_mfma_f32_16x16x32_f16 v[28:31], v[132:135], v[116:119], v[28:31]
	s_waitcnt lgkmcnt(0)
	v_mfma_f32_16x16x32_f16 v[60:63], v[14:17], v[136:139], v[60:63]
	v_mfma_f32_16x16x32_f16 v[68:71], v[20:23], v[136:139], v[68:71]
	v_mfma_f32_16x16x32_f16 v[32:35], v[136:139], v[116:119], v[32:35]
	ds_read_b128 v[132:135], v57 offset:28672
	ds_read_b128 v[136:139], v57 offset:30720
	s_waitcnt lgkmcnt(1)
	v_mfma_f32_16x16x32_f16 v[88:91], v[14:17], v[132:135], v[88:91]
	v_mfma_f32_16x16x32_f16 v[96:99], v[20:23], v[132:135], v[96:99]
	s_waitcnt lgkmcnt(0)
	v_mfma_f32_16x16x32_f16 v[6:9], v[14:17], v[136:139], v[6:9]
	v_mfma_f32_16x16x32_f16 v[10:13], v[20:23], v[136:139], v[10:13]
	ds_read_b128 v[14:17], v58 offset:24576
	ds_read_b128 v[20:23], v58 offset:26624
	s_waitcnt vmcnt(14) lgkmcnt(1)
	v_mfma_f32_16x16x32_f16 v[24:27], v[120:123], v[14:17], v[24:27]
	s_waitcnt vmcnt(13)
	v_mfma_f32_16x16x32_f16 v[36:39], v[124:127], v[14:17], v[36:39]
	s_waitcnt vmcnt(12)
	v_mfma_f32_16x16x32_f16 v[14:17], v[14:17], v[128:131], v[28:31]
	s_waitcnt lgkmcnt(0)
	v_mfma_f32_16x16x32_f16 v[28:31], v[120:123], v[20:23], v[60:63]
	v_mfma_f32_16x16x32_f16 v[60:63], v[124:127], v[20:23], v[68:71]
	v_mfma_f32_16x16x32_f16 v[20:23], v[20:23], v[128:131], v[32:35]
	s_nop 2
	ds_read_b128 v[32:35], v58 offset:28672
	ds_read_b128 v[68:71], v58 offset:30720
	v_mfma_f32_16x16x32_f16 v[64:67], v[132:135], v[116:119], v[64:67]
	v_mfma_f32_16x16x32_f16 v[2:5], v[136:139], v[116:119], v[2:5]
	s_waitcnt lgkmcnt(1)
	v_mfma_f32_16x16x32_f16 v[88:91], v[120:123], v[32:35], v[88:91]
	v_mfma_f32_16x16x32_f16 v[96:99], v[124:127], v[32:35], v[96:99]
	v_mfma_f32_16x16x32_f16 v[32:35], v[32:35], v[128:131], v[64:67]
	s_waitcnt lgkmcnt(0)
	v_mfma_f32_16x16x32_f16 v[6:9], v[120:123], v[68:71], v[6:9]
	v_mfma_f32_16x16x32_f16 v[10:13], v[124:127], v[68:71], v[10:13]
	v_mfma_f32_16x16x32_f16 v[2:5], v[68:71], v[128:131], v[2:5]
	global_load_dwordx4 v[64:67], v[52:53], off
	global_load_dwordx4 v[68:71], v[52:53], off offset:1024
	global_load_dwordx4 v[116:119], v[52:53], off offset:2048
	global_load_dwordx4 v[120:123], v[52:53], off offset:3072
	v_add_co_u32_e32 v52, vcc, s2, v52
	s_nop 1
	v_addc_co_u32_e32 v53, vcc, 0, v53, vcc
	global_load_dwordx4 v[124:127], v[52:53], off
	global_load_dwordx4 v[128:131], v[52:53], off offset:1024
	s_barrier
	ds_read_b128 v[132:135], v57 offset:32768
	ds_read_b128 v[136:139], v57 offset:34816
	s_waitcnt vmcnt(17) lgkmcnt(1)
	v_mfma_f32_16x16x32_f16 v[24:27], v[40:43], v[132:135], v[24:27]
	v_lshl_add_u64 v[52:53], v[18:19], 0, s[14:15]
	s_mul_i32 s14, s4, 0x1800
	s_add_i32 s4, s3, 9
	s_waitcnt vmcnt(16)
	v_mfma_f32_16x16x32_f16 v[36:39], v[44:47], v[132:135], v[36:39]
	s_and_b32 s4, s4, 15
	s_waitcnt vmcnt(15)
	v_mfma_f32_16x16x32_f16 v[14:17], v[132:135], v[48:51], v[14:17]
	s_waitcnt lgkmcnt(0)
	v_mfma_f32_16x16x32_f16 v[28:31], v[40:43], v[136:139], v[28:31]
	v_mfma_f32_16x16x32_f16 v[60:63], v[44:47], v[136:139], v[60:63]
	v_mfma_f32_16x16x32_f16 v[20:23], v[136:139], v[48:51], v[20:23]
	ds_read_b128 v[132:135], v57 offset:36864
	ds_read_b128 v[136:139], v57 offset:38912
	s_waitcnt lgkmcnt(1)
	v_mfma_f32_16x16x32_f16 v[88:91], v[40:43], v[132:135], v[88:91]
	v_mfma_f32_16x16x32_f16 v[96:99], v[44:47], v[132:135], v[96:99]
	s_waitcnt lgkmcnt(0)
	v_mfma_f32_16x16x32_f16 v[6:9], v[40:43], v[136:139], v[6:9]
	v_mfma_f32_16x16x32_f16 v[10:13], v[44:47], v[136:139], v[10:13]
	ds_read_b128 v[40:43], v58 offset:32768
	ds_read_b128 v[44:47], v58 offset:34816
	v_mfma_f32_16x16x32_f16 v[32:35], v[132:135], v[48:51], v[32:35]
	v_mfma_f32_16x16x32_f16 v[2:5], v[136:139], v[48:51], v[2:5]
	s_waitcnt vmcnt(14) lgkmcnt(1)
	v_mfma_f32_16x16x32_f16 v[24:27], v[100:103], v[40:43], v[24:27]
	s_waitcnt vmcnt(13)
	v_mfma_f32_16x16x32_f16 v[36:39], v[108:111], v[40:43], v[36:39]
	s_waitcnt vmcnt(12)
	v_mfma_f32_16x16x32_f16 v[14:17], v[40:43], v[112:115], v[14:17]
	s_waitcnt lgkmcnt(0)
	v_mfma_f32_16x16x32_f16 v[28:31], v[100:103], v[44:47], v[28:31]
	v_mfma_f32_16x16x32_f16 v[40:43], v[108:111], v[44:47], v[60:63]
	v_mfma_f32_16x16x32_f16 v[20:23], v[44:47], v[112:115], v[20:23]
	ds_read_b128 v[44:47], v58 offset:36864
	ds_read_b128 v[48:51], v58 offset:38912
	s_waitcnt lgkmcnt(1)
	v_mfma_f32_16x16x32_f16 v[60:63], v[100:103], v[44:47], v[88:91]
	v_mfma_f32_16x16x32_f16 v[88:91], v[108:111], v[44:47], v[96:99]
	v_mfma_f32_16x16x32_f16 v[32:35], v[44:47], v[112:115], v[32:35]
	s_waitcnt lgkmcnt(0)
	v_mfma_f32_16x16x32_f16 v[6:9], v[100:103], v[48:51], v[6:9]
	v_mfma_f32_16x16x32_f16 v[10:13], v[108:111], v[48:51], v[10:13]
	v_mfma_f32_16x16x32_f16 v[2:5], v[48:51], v[112:115], v[2:5]
	global_load_dwordx4 v[44:47], v[52:53], off
	global_load_dwordx4 v[48:51], v[52:53], off offset:1024
	global_load_dwordx4 v[96:99], v[52:53], off offset:2048
	global_load_dwordx4 v[100:103], v[52:53], off offset:3072
	v_add_co_u32_e32 v52, vcc, s2, v52
	s_nop 1
	v_addc_co_u32_e32 v53, vcc, 0, v53, vcc
	global_load_dwordx4 v[108:111], v[52:53], off
	global_load_dwordx4 v[112:115], v[52:53], off offset:1024
	s_barrier
	ds_read_b128 v[132:135], v57 offset:40960
	ds_read_b128 v[136:139], v57 offset:43008
	s_waitcnt vmcnt(17) lgkmcnt(1)
	v_mfma_f32_16x16x32_f16 v[24:27], v[72:75], v[132:135], v[24:27]
	v_lshl_add_u64 v[52:53], v[18:19], 0, s[14:15]
	s_mul_i32 s14, s4, 0x1800
	s_add_i32 s4, s3, 10
	s_waitcnt vmcnt(16)
	v_mfma_f32_16x16x32_f16 v[36:39], v[76:79], v[132:135], v[36:39]
	s_and_b32 s4, s4, 15
	s_waitcnt vmcnt(15)
	v_mfma_f32_16x16x32_f16 v[14:17], v[132:135], v[80:83], v[14:17]
	s_waitcnt lgkmcnt(0)
	v_mfma_f32_16x16x32_f16 v[28:31], v[72:75], v[136:139], v[28:31]
	v_mfma_f32_16x16x32_f16 v[40:43], v[76:79], v[136:139], v[40:43]
	v_mfma_f32_16x16x32_f16 v[20:23], v[136:139], v[80:83], v[20:23]
	ds_read_b128 v[132:135], v57 offset:45056
	ds_read_b128 v[136:139], v57 offset:47104
	s_waitcnt lgkmcnt(1)
	v_mfma_f32_16x16x32_f16 v[60:63], v[72:75], v[132:135], v[60:63]
	v_mfma_f32_16x16x32_f16 v[88:91], v[76:79], v[132:135], v[88:91]
	s_waitcnt lgkmcnt(0)
	v_mfma_f32_16x16x32_f16 v[6:9], v[72:75], v[136:139], v[6:9]
	v_mfma_f32_16x16x32_f16 v[10:13], v[76:79], v[136:139], v[10:13]
	ds_read_b128 v[72:75], v58 offset:40960
	ds_read_b128 v[76:79], v58 offset:43008
	s_waitcnt vmcnt(14) lgkmcnt(1)
	v_mfma_f32_16x16x32_f16 v[24:27], v[84:87], v[72:75], v[24:27]
	s_waitcnt vmcnt(13)
	v_mfma_f32_16x16x32_f16 v[36:39], v[92:95], v[72:75], v[36:39]
	s_waitcnt vmcnt(12)
	v_mfma_f32_16x16x32_f16 v[14:17], v[72:75], v[104:107], v[14:17]
	s_waitcnt lgkmcnt(0)
	v_mfma_f32_16x16x32_f16 v[28:31], v[84:87], v[76:79], v[28:31]
	v_mfma_f32_16x16x32_f16 v[40:43], v[92:95], v[76:79], v[40:43]
	v_mfma_f32_16x16x32_f16 v[20:23], v[76:79], v[104:107], v[20:23]
	ds_read_b128 v[72:75], v58 offset:45056
	ds_read_b128 v[76:79], v58 offset:47104
	v_mfma_f32_16x16x32_f16 v[32:35], v[132:135], v[80:83], v[32:35]
	v_mfma_f32_16x16x32_f16 v[2:5], v[136:139], v[80:83], v[2:5]
	s_waitcnt lgkmcnt(1)
	v_mfma_f32_16x16x32_f16 v[60:63], v[84:87], v[72:75], v[60:63]
	v_mfma_f32_16x16x32_f16 v[80:83], v[92:95], v[72:75], v[88:91]
	v_mfma_f32_16x16x32_f16 v[32:35], v[72:75], v[104:107], v[32:35]
	s_waitcnt lgkmcnt(0)
	v_mfma_f32_16x16x32_f16 v[6:9], v[84:87], v[76:79], v[6:9]
	v_mfma_f32_16x16x32_f16 v[10:13], v[92:95], v[76:79], v[10:13]
	v_mfma_f32_16x16x32_f16 v[2:5], v[76:79], v[104:107], v[2:5]
	global_load_dwordx4 v[72:75], v[52:53], off
	global_load_dwordx4 v[76:79], v[52:53], off offset:1024
	global_load_dwordx4 v[84:87], v[52:53], off offset:2048
	global_load_dwordx4 v[88:91], v[52:53], off offset:3072
	v_add_co_u32_e32 v52, vcc, s2, v52
	s_nop 1
	v_addc_co_u32_e32 v53, vcc, 0, v53, vcc
	global_load_dwordx4 v[92:95], v[52:53], off
	global_load_dwordx4 v[104:107], v[52:53], off offset:1024
	s_barrier
	ds_read_b128 v[132:135], v57 offset:49152
	ds_read_b128 v[136:139], v57 offset:51200
	s_waitcnt vmcnt(17) lgkmcnt(1)
	v_mfma_f32_16x16x32_f16 v[24:27], v[64:67], v[132:135], v[24:27]
	v_lshl_add_u64 v[52:53], v[18:19], 0, s[14:15]
	s_mul_i32 s14, s4, 0x1800
	s_add_i32 s4, s3, 11
	s_waitcnt vmcnt(16)
	v_mfma_f32_16x16x32_f16 v[36:39], v[68:71], v[132:135], v[36:39]
	s_and_b32 s4, s4, 15
	s_waitcnt vmcnt(15)
	v_mfma_f32_16x16x32_f16 v[14:17], v[132:135], v[116:119], v[14:17]
	s_waitcnt lgkmcnt(0)
	v_mfma_f32_16x16x32_f16 v[28:31], v[64:67], v[136:139], v[28:31]
	v_mfma_f32_16x16x32_f16 v[40:43], v[68:71], v[136:139], v[40:43]
	v_mfma_f32_16x16x32_f16 v[20:23], v[136:139], v[116:119], v[20:23]
	ds_read_b128 v[132:135], v57 offset:53248
	ds_read_b128 v[136:139], v57 offset:55296
	s_waitcnt lgkmcnt(1)
	v_mfma_f32_16x16x32_f16 v[60:63], v[64:67], v[132:135], v[60:63]
	v_mfma_f32_16x16x32_f16 v[80:83], v[68:71], v[132:135], v[80:83]
	s_waitcnt lgkmcnt(0)
	v_mfma_f32_16x16x32_f16 v[6:9], v[64:67], v[136:139], v[6:9]
	v_mfma_f32_16x16x32_f16 v[10:13], v[68:71], v[136:139], v[10:13]
	ds_read_b128 v[64:67], v58 offset:49152
	ds_read_b128 v[68:71], v58 offset:51200
	s_waitcnt vmcnt(14) lgkmcnt(1)
	v_mfma_f32_16x16x32_f16 v[24:27], v[120:123], v[64:67], v[24:27]
	s_waitcnt vmcnt(13)
	v_mfma_f32_16x16x32_f16 v[36:39], v[124:127], v[64:67], v[36:39]
	s_waitcnt vmcnt(12)
	v_mfma_f32_16x16x32_f16 v[14:17], v[64:67], v[128:131], v[14:17]
	s_waitcnt lgkmcnt(0)
	v_mfma_f32_16x16x32_f16 v[28:31], v[120:123], v[68:71], v[28:31]
	v_mfma_f32_16x16x32_f16 v[40:43], v[124:127], v[68:71], v[40:43]
	v_mfma_f32_16x16x32_f16 v[20:23], v[68:71], v[128:131], v[20:23]
	ds_read_b128 v[64:67], v58 offset:53248
	ds_read_b128 v[68:71], v58 offset:55296
	v_mfma_f32_16x16x32_f16 v[32:35], v[132:135], v[116:119], v[32:35]
	v_mfma_f32_16x16x32_f16 v[2:5], v[136:139], v[116:119], v[2:5]
	s_waitcnt lgkmcnt(1)
	v_mfma_f32_16x16x32_f16 v[60:63], v[120:123], v[64:67], v[60:63]
	v_mfma_f32_16x16x32_f16 v[80:83], v[124:127], v[64:67], v[80:83]
	v_mfma_f32_16x16x32_f16 v[32:35], v[64:67], v[128:131], v[32:35]
	s_waitcnt lgkmcnt(0)
	v_mfma_f32_16x16x32_f16 v[6:9], v[120:123], v[68:71], v[6:9]
	v_mfma_f32_16x16x32_f16 v[10:13], v[124:127], v[68:71], v[10:13]
	v_mfma_f32_16x16x32_f16 v[2:5], v[68:71], v[128:131], v[2:5]
	global_load_dwordx4 v[64:67], v[52:53], off
	global_load_dwordx4 v[68:71], v[52:53], off offset:1024
	global_load_dwordx4 v[116:119], v[52:53], off offset:2048
	global_load_dwordx4 v[120:123], v[52:53], off offset:3072
	v_add_co_u32_e32 v52, vcc, s2, v52
	s_nop 1
	v_addc_co_u32_e32 v53, vcc, 0, v53, vcc
	global_load_dwordx4 v[124:127], v[52:53], off
	global_load_dwordx4 v[128:131], v[52:53], off offset:1024
	s_barrier
	ds_read_b128 v[132:135], v57 offset:57344
	ds_read_b128 v[136:139], v57 offset:59392
	s_waitcnt vmcnt(17) lgkmcnt(1)
	v_mfma_f32_16x16x32_f16 v[24:27], v[44:47], v[132:135], v[24:27]
	v_lshl_add_u64 v[52:53], v[18:19], 0, s[14:15]
	s_mul_i32 s14, s4, 0x1800
	s_add_i32 s4, s3, 12
	s_waitcnt vmcnt(16)
	v_mfma_f32_16x16x32_f16 v[36:39], v[48:51], v[132:135], v[36:39]
	s_and_b32 s4, s4, 15
	s_waitcnt vmcnt(15)
	v_mfma_f32_16x16x32_f16 v[14:17], v[132:135], v[96:99], v[14:17]
	s_waitcnt lgkmcnt(0)
	v_mfma_f32_16x16x32_f16 v[28:31], v[44:47], v[136:139], v[28:31]
	v_mfma_f32_16x16x32_f16 v[40:43], v[48:51], v[136:139], v[40:43]
	v_mfma_f32_16x16x32_f16 v[20:23], v[136:139], v[96:99], v[20:23]
	ds_read_b128 v[132:135], v57 offset:61440
	ds_read_b128 v[136:139], v57 offset:63488
	s_waitcnt lgkmcnt(1)
	v_mfma_f32_16x16x32_f16 v[60:63], v[44:47], v[132:135], v[60:63]
	v_mfma_f32_16x16x32_f16 v[80:83], v[48:51], v[132:135], v[80:83]
	s_waitcnt lgkmcnt(0)
	v_mfma_f32_16x16x32_f16 v[6:9], v[44:47], v[136:139], v[6:9]
	v_mfma_f32_16x16x32_f16 v[10:13], v[48:51], v[136:139], v[10:13]
	ds_read_b128 v[44:47], v58 offset:57344
	ds_read_b128 v[48:51], v58 offset:59392
	s_waitcnt vmcnt(14) lgkmcnt(1)
	v_mfma_f32_16x16x32_f16 v[24:27], v[100:103], v[44:47], v[24:27]
	s_waitcnt vmcnt(13)
	v_mfma_f32_16x16x32_f16 v[36:39], v[108:111], v[44:47], v[36:39]
	s_waitcnt vmcnt(12)
	v_mfma_f32_16x16x32_f16 v[14:17], v[44:47], v[112:115], v[14:17]
	s_waitcnt lgkmcnt(0)
	v_mfma_f32_16x16x32_f16 v[28:31], v[100:103], v[48:51], v[28:31]
	v_mfma_f32_16x16x32_f16 v[40:43], v[108:111], v[48:51], v[40:43]
	v_mfma_f32_16x16x32_f16 v[20:23], v[48:51], v[112:115], v[20:23]
	ds_read_b128 v[44:47], v58 offset:61440
	ds_read_b128 v[48:51], v58 offset:63488
	v_mfma_f32_16x16x32_f16 v[32:35], v[132:135], v[96:99], v[32:35]
	v_mfma_f32_16x16x32_f16 v[2:5], v[136:139], v[96:99], v[2:5]
	s_waitcnt lgkmcnt(1)
	v_mfma_f32_16x16x32_f16 v[60:63], v[100:103], v[44:47], v[60:63]
	v_mfma_f32_16x16x32_f16 v[80:83], v[108:111], v[44:47], v[80:83]
	v_mfma_f32_16x16x32_f16 v[32:35], v[44:47], v[112:115], v[32:35]
	s_waitcnt lgkmcnt(0)
	v_mfma_f32_16x16x32_f16 v[6:9], v[100:103], v[48:51], v[6:9]
	v_mfma_f32_16x16x32_f16 v[10:13], v[108:111], v[48:51], v[10:13]
	v_mfma_f32_16x16x32_f16 v[2:5], v[48:51], v[112:115], v[2:5]
	global_load_dwordx4 v[44:47], v[52:53], off
	global_load_dwordx4 v[48:51], v[52:53], off offset:1024
	global_load_dwordx4 v[96:99], v[52:53], off offset:2048
	global_load_dwordx4 v[100:103], v[52:53], off offset:3072
	v_add_co_u32_e32 v52, vcc, s2, v52
	s_nop 1
	v_addc_co_u32_e32 v53, vcc, 0, v53, vcc
	global_load_dwordx4 v[108:111], v[52:53], off
	global_load_dwordx4 v[112:115], v[52:53], off offset:1024
	v_or_b32_e32 v52, 0x10000, v57
	s_barrier
	ds_read_b128 v[132:135], v52
	v_or_b32_e32 v52, 0x10800, v57
	ds_read_b128 v[136:139], v52
	v_or_b32_e32 v52, 0x11000, v57
	s_waitcnt vmcnt(17) lgkmcnt(1)
	v_mfma_f32_16x16x32_f16 v[24:27], v[72:75], v[132:135], v[24:27]
	s_waitcnt vmcnt(16)
	v_mfma_f32_16x16x32_f16 v[36:39], v[76:79], v[132:135], v[36:39]
	s_waitcnt vmcnt(15)
	v_mfma_f32_16x16x32_f16 v[14:17], v[132:135], v[84:87], v[14:17]
	ds_read_b128 v[132:135], v52
	v_or_b32_e32 v52, 0x11800, v57
	s_waitcnt lgkmcnt(1)
	v_mfma_f32_16x16x32_f16 v[28:31], v[72:75], v[136:139], v[28:31]
	v_mfma_f32_16x16x32_f16 v[40:43], v[76:79], v[136:139], v[40:43]
	v_mfma_f32_16x16x32_f16 v[20:23], v[136:139], v[84:87], v[20:23]
	ds_read_b128 v[136:139], v52
	v_or_b32_e32 v52, 0x10000, v58
	s_waitcnt lgkmcnt(1)
	v_mfma_f32_16x16x32_f16 v[60:63], v[72:75], v[132:135], v[60:63]
	s_waitcnt lgkmcnt(0)
	v_mfma_f32_16x16x32_f16 v[6:9], v[72:75], v[136:139], v[6:9]
	ds_read_b128 v[72:75], v52
	v_or_b32_e32 v52, 0x10800, v58
	v_mfma_f32_16x16x32_f16 v[80:83], v[76:79], v[132:135], v[80:83]
	v_mfma_f32_16x16x32_f16 v[10:13], v[76:79], v[136:139], v[10:13]
	ds_read_b128 v[76:79], v52
	v_or_b32_e32 v52, 0x11000, v58
	s_waitcnt vmcnt(14) lgkmcnt(1)
	v_mfma_f32_16x16x32_f16 v[24:27], v[88:91], v[72:75], v[24:27]
	s_waitcnt vmcnt(13)
	v_mfma_f32_16x16x32_f16 v[36:39], v[92:95], v[72:75], v[36:39]
	s_waitcnt vmcnt(12)
	v_mfma_f32_16x16x32_f16 v[14:17], v[72:75], v[104:107], v[14:17]
	ds_read_b128 v[72:75], v52
	v_or_b32_e32 v52, 0x11800, v58
	s_waitcnt lgkmcnt(1)
	v_mfma_f32_16x16x32_f16 v[28:31], v[88:91], v[76:79], v[28:31]
	v_mfma_f32_16x16x32_f16 v[40:43], v[92:95], v[76:79], v[40:43]
	v_mfma_f32_16x16x32_f16 v[20:23], v[76:79], v[104:107], v[20:23]
	ds_read_b128 v[76:79], v52
	v_lshl_add_u64 v[52:53], v[18:19], 0, s[14:15]
	s_mul_i32 s14, s4, 0x1800
	v_mfma_f32_16x16x32_f16 v[32:35], v[132:135], v[84:87], v[32:35]
	s_add_i32 s4, s3, 13
	s_and_b32 s4, s4, 15
	v_mfma_f32_16x16x32_f16 v[2:5], v[136:139], v[84:87], v[2:5]
	s_waitcnt lgkmcnt(1)
	v_mfma_f32_16x16x32_f16 v[60:63], v[88:91], v[72:75], v[60:63]
	v_mfma_f32_16x16x32_f16 v[80:83], v[92:95], v[72:75], v[80:83]
	v_mfma_f32_16x16x32_f16 v[32:35], v[72:75], v[104:107], v[32:35]
	s_waitcnt lgkmcnt(0)
	v_mfma_f32_16x16x32_f16 v[6:9], v[88:91], v[76:79], v[6:9]
	v_mfma_f32_16x16x32_f16 v[10:13], v[92:95], v[76:79], v[10:13]
	v_mfma_f32_16x16x32_f16 v[2:5], v[76:79], v[104:107], v[2:5]
	global_load_dwordx4 v[72:75], v[52:53], off
	global_load_dwordx4 v[76:79], v[52:53], off offset:1024
	global_load_dwordx4 v[84:87], v[52:53], off offset:2048
	global_load_dwordx4 v[88:91], v[52:53], off offset:3072
	v_add_co_u32_e32 v52, vcc, s2, v52
	s_nop 1
	v_addc_co_u32_e32 v53, vcc, 0, v53, vcc
	global_load_dwordx4 v[92:95], v[52:53], off
	global_load_dwordx4 v[104:107], v[52:53], off offset:1024
	v_or_b32_e32 v52, 0x12000, v57
	s_barrier
	ds_read_b128 v[132:135], v52
	v_or_b32_e32 v52, 0x12800, v57
	ds_read_b128 v[136:139], v52
	v_or_b32_e32 v52, 0x13000, v57
	s_waitcnt vmcnt(17) lgkmcnt(1)
	v_mfma_f32_16x16x32_f16 v[24:27], v[64:67], v[132:135], v[24:27]
	s_waitcnt vmcnt(16)
	v_mfma_f32_16x16x32_f16 v[36:39], v[68:71], v[132:135], v[36:39]
	s_waitcnt vmcnt(15)
	v_mfma_f32_16x16x32_f16 v[14:17], v[132:135], v[116:119], v[14:17]
	ds_read_b128 v[132:135], v52
	v_or_b32_e32 v52, 0x13800, v57
	s_waitcnt lgkmcnt(1)
	v_mfma_f32_16x16x32_f16 v[28:31], v[64:67], v[136:139], v[28:31]
	v_mfma_f32_16x16x32_f16 v[40:43], v[68:71], v[136:139], v[40:43]
	v_mfma_f32_16x16x32_f16 v[20:23], v[136:139], v[116:119], v[20:23]
	ds_read_b128 v[136:139], v52
	v_or_b32_e32 v52, 0x12000, v58
	s_waitcnt lgkmcnt(1)
	v_mfma_f32_16x16x32_f16 v[60:63], v[64:67], v[132:135], v[60:63]
	s_waitcnt lgkmcnt(0)
	v_mfma_f32_16x16x32_f16 v[6:9], v[64:67], v[136:139], v[6:9]
	ds_read_b128 v[64:67], v52
	v_or_b32_e32 v52, 0x12800, v58
	v_mfma_f32_16x16x32_f16 v[80:83], v[68:71], v[132:135], v[80:83]
	v_mfma_f32_16x16x32_f16 v[10:13], v[68:71], v[136:139], v[10:13]
	ds_read_b128 v[68:71], v52
	v_or_b32_e32 v52, 0x13000, v58
	s_waitcnt vmcnt(14) lgkmcnt(1)
	v_mfma_f32_16x16x32_f16 v[24:27], v[120:123], v[64:67], v[24:27]
	s_waitcnt vmcnt(13)
	v_mfma_f32_16x16x32_f16 v[36:39], v[124:127], v[64:67], v[36:39]
	s_waitcnt vmcnt(12)
	v_mfma_f32_16x16x32_f16 v[14:17], v[64:67], v[128:131], v[14:17]
	ds_read_b128 v[64:67], v52
	v_or_b32_e32 v52, 0x13800, v58
	s_waitcnt lgkmcnt(1)
	v_mfma_f32_16x16x32_f16 v[28:31], v[120:123], v[68:71], v[28:31]
	v_mfma_f32_16x16x32_f16 v[40:43], v[124:127], v[68:71], v[40:43]
	v_mfma_f32_16x16x32_f16 v[20:23], v[68:71], v[128:131], v[20:23]
	ds_read_b128 v[68:71], v52
	v_lshl_add_u64 v[52:53], v[18:19], 0, s[14:15]
	s_mul_i32 s14, s4, 0x1800
	v_mfma_f32_16x16x32_f16 v[32:35], v[132:135], v[116:119], v[32:35]
	s_add_i32 s4, s3, 14
	s_and_b32 s4, s4, 15
	v_mfma_f32_16x16x32_f16 v[2:5], v[136:139], v[116:119], v[2:5]
	s_waitcnt lgkmcnt(1)
	v_mfma_f32_16x16x32_f16 v[60:63], v[120:123], v[64:67], v[60:63]
	v_mfma_f32_16x16x32_f16 v[80:83], v[124:127], v[64:67], v[80:83]
	v_mfma_f32_16x16x32_f16 v[32:35], v[64:67], v[128:131], v[32:35]
	s_waitcnt lgkmcnt(0)
	v_mfma_f32_16x16x32_f16 v[6:9], v[120:123], v[68:71], v[6:9]
	v_mfma_f32_16x16x32_f16 v[10:13], v[124:127], v[68:71], v[10:13]
	v_mfma_f32_16x16x32_f16 v[2:5], v[68:71], v[128:131], v[2:5]
	global_load_dwordx4 v[64:67], v[52:53], off
	global_load_dwordx4 v[68:71], v[52:53], off offset:1024
	global_load_dwordx4 v[116:119], v[52:53], off offset:2048
	global_load_dwordx4 v[120:123], v[52:53], off offset:3072
	v_add_co_u32_e32 v52, vcc, s2, v52
	s_nop 1
	v_addc_co_u32_e32 v53, vcc, 0, v53, vcc
	global_load_dwordx4 v[124:127], v[52:53], off
	global_load_dwordx4 v[128:131], v[52:53], off offset:1024
	v_or_b32_e32 v52, 0x14000, v57
	s_barrier
	ds_read_b128 v[132:135], v52
	v_or_b32_e32 v52, 0x14800, v57
	ds_read_b128 v[136:139], v52
	v_or_b32_e32 v52, 0x15000, v57
	s_waitcnt vmcnt(17) lgkmcnt(1)
	v_mfma_f32_16x16x32_f16 v[24:27], v[44:47], v[132:135], v[24:27]
	s_waitcnt vmcnt(16)
	v_mfma_f32_16x16x32_f16 v[36:39], v[48:51], v[132:135], v[36:39]
	s_waitcnt vmcnt(15)
	v_mfma_f32_16x16x32_f16 v[14:17], v[132:135], v[96:99], v[14:17]
	ds_read_b128 v[132:135], v52
	v_or_b32_e32 v52, 0x15800, v57
	s_waitcnt lgkmcnt(1)
	v_mfma_f32_16x16x32_f16 v[28:31], v[44:47], v[136:139], v[28:31]
	v_mfma_f32_16x16x32_f16 v[40:43], v[48:51], v[136:139], v[40:43]
	v_mfma_f32_16x16x32_f16 v[20:23], v[136:139], v[96:99], v[20:23]
	ds_read_b128 v[136:139], v52
	s_waitcnt lgkmcnt(1)
	v_mfma_f32_16x16x32_f16 v[60:63], v[44:47], v[132:135], v[60:63]
	s_waitcnt lgkmcnt(0)
	v_mfma_f32_16x16x32_f16 v[6:9], v[44:47], v[136:139], v[6:9]
	v_or_b32_e32 v44, 0x14000, v58
	ds_read_b128 v[44:47], v44
	v_mfma_f32_16x16x32_f16 v[80:83], v[48:51], v[132:135], v[80:83]
	v_mfma_f32_16x16x32_f16 v[10:13], v[48:51], v[136:139], v[10:13]
	v_or_b32_e32 v48, 0x14800, v58
	ds_read_b128 v[48:51], v48
	s_waitcnt vmcnt(14) lgkmcnt(1)
	v_mfma_f32_16x16x32_f16 v[24:27], v[100:103], v[44:47], v[24:27]
	s_waitcnt vmcnt(13)
	v_mfma_f32_16x16x32_f16 v[36:39], v[108:111], v[44:47], v[36:39]
	s_waitcnt vmcnt(12)
	v_mfma_f32_16x16x32_f16 v[14:17], v[44:47], v[112:115], v[14:17]
	v_or_b32_e32 v44, 0x15000, v58
	ds_read_b128 v[44:47], v44
	s_waitcnt lgkmcnt(1)
	v_mfma_f32_16x16x32_f16 v[28:31], v[100:103], v[48:51], v[28:31]
	v_mfma_f32_16x16x32_f16 v[40:43], v[108:111], v[48:51], v[40:43]
	v_mfma_f32_16x16x32_f16 v[20:23], v[48:51], v[112:115], v[20:23]
	v_or_b32_e32 v48, 0x15800, v58
	ds_read_b128 v[48:51], v48
	v_mfma_f32_16x16x32_f16 v[32:35], v[132:135], v[96:99], v[32:35]
	v_mfma_f32_16x16x32_f16 v[2:5], v[136:139], v[96:99], v[2:5]
	s_waitcnt lgkmcnt(1)
	v_mfma_f32_16x16x32_f16 v[60:63], v[100:103], v[44:47], v[60:63]
	v_mfma_f32_16x16x32_f16 v[80:83], v[108:111], v[44:47], v[80:83]
	v_mfma_f32_16x16x32_f16 v[32:35], v[44:47], v[112:115], v[32:35]
	v_lshl_add_u64 v[44:45], v[18:19], 0, s[14:15]
	s_mul_i32 s14, s4, 0x1800
	s_add_i32 s4, s3, -1
	s_waitcnt lgkmcnt(0)
	v_mfma_f32_16x16x32_f16 v[6:9], v[100:103], v[48:51], v[6:9]
	s_and_b32 s4, s4, 15
	v_mfma_f32_16x16x32_f16 v[10:13], v[108:111], v[48:51], v[10:13]
	v_mfma_f32_16x16x32_f16 v[2:5], v[48:51], v[112:115], v[2:5]
	global_load_dwordx4 v[50:53], v[44:45], off
	global_load_dwordx4 v[96:99], v[44:45], off offset:1024
	global_load_dwordx4 v[100:103], v[44:45], off offset:2048
	global_load_dwordx4 v[108:111], v[44:45], off offset:3072
	v_add_co_u32_e32 v44, vcc, s2, v44
	v_or_b32_e32 v48, 0x16800, v57
	s_nop 0
	v_addc_co_u32_e32 v45, vcc, 0, v45, vcc
	global_load_dwordx4 v[112:115], v[44:45], off
	global_load_dwordx4 v[132:135], v[44:45], off offset:1024
	v_or_b32_e32 v44, 0x16000, v57
	s_barrier
	ds_read_b128 v[44:47], v44
	ds_read_b128 v[136:139], v48
	s_waitcnt vmcnt(17) lgkmcnt(1)
	v_mfma_f32_16x16x32_f16 v[24:27], v[72:75], v[44:47], v[24:27]
	v_or_b32_e32 v48, 0x17800, v57
	s_waitcnt vmcnt(16)
	v_mfma_f32_16x16x32_f16 v[36:39], v[76:79], v[44:47], v[36:39]
	s_waitcnt vmcnt(15)
	v_mfma_f32_16x16x32_f16 v[14:17], v[44:47], v[84:87], v[14:17]
	v_or_b32_e32 v44, 0x17000, v57
	ds_read_b128 v[44:47], v44
	s_waitcnt lgkmcnt(1)
	v_mfma_f32_16x16x32_f16 v[28:31], v[72:75], v[136:139], v[28:31]
	v_mfma_f32_16x16x32_f16 v[40:43], v[76:79], v[136:139], v[40:43]
	v_mfma_f32_16x16x32_f16 v[20:23], v[136:139], v[84:87], v[20:23]
	ds_read_b128 v[136:139], v48
	v_or_b32_e32 v48, 0x16800, v58
	s_waitcnt lgkmcnt(1)
	v_mfma_f32_16x16x32_f16 v[60:63], v[72:75], v[44:47], v[60:63]
	v_mfma_f32_16x16x32_f16 v[80:83], v[76:79], v[44:47], v[80:83]
	v_mfma_f32_16x16x32_f16 v[32:35], v[44:47], v[84:87], v[32:35]
	v_or_b32_e32 v44, 0x16000, v58
	ds_read_b128 v[44:47], v44
	s_waitcnt lgkmcnt(1)
	v_mfma_f32_16x16x32_f16 v[6:9], v[72:75], v[136:139], v[6:9]
	ds_read_b128 v[72:75], v48
	v_mfma_f32_16x16x32_f16 v[10:13], v[76:79], v[136:139], v[10:13]
	v_mfma_f32_16x16x32_f16 v[2:5], v[136:139], v[84:87], v[2:5]
	s_waitcnt vmcnt(12) lgkmcnt(1)
	v_mfma_f32_16x16x32_f16 v[76:79], v[44:47], v[104:107], v[14:17]
	s_waitcnt lgkmcnt(0)
	v_mfma_f32_16x16x32_f16 v[84:87], v[92:95], v[72:75], v[40:43]
	s_nop 0
	v_or_b32_e32 v14, 0x17000, v58
	ds_read_b128 v[14:17], v14
	v_or_b32_e32 v40, 0x17800, v58
	ds_read_b128 v[40:43], v40
	v_mfma_f32_16x16x32_f16 v[24:27], v[88:91], v[44:47], v[24:27]
	v_mfma_f32_16x16x32_f16 v[36:39], v[92:95], v[44:47], v[36:39]
	v_mfma_f32_16x16x32_f16 v[28:31], v[88:91], v[72:75], v[28:31]
	v_mfma_f32_16x16x32_f16 v[20:23], v[72:75], v[104:107], v[20:23]
	s_waitcnt lgkmcnt(1)
	v_mfma_f32_16x16x32_f16 v[60:63], v[88:91], v[14:17], v[60:63]
	v_mfma_f32_16x16x32_f16 v[72:75], v[92:95], v[14:17], v[80:83]
	s_waitcnt lgkmcnt(0)
	v_mfma_f32_16x16x32_f16 v[80:83], v[88:91], v[40:43], v[6:9]
	v_mfma_f32_16x16x32_f16 v[88:91], v[92:95], v[40:43], v[10:13]
	v_mfma_f32_16x16x32_f16 v[92:95], v[40:43], v[104:107], v[2:5]
	v_or_b32_e32 v40, 0x18000, v57
	s_nop 1
	v_lshl_add_u64 v[2:3], v[18:19], 0, s[14:15]
	v_mfma_f32_16x16x32_f16 v[32:35], v[14:17], v[104:107], v[32:35]
	global_load_dwordx4 v[46:49], v[2:3], off
	global_load_dwordx4 v[42:45], v[2:3], off offset:1024
	global_load_dwordx4 v[14:17], v[2:3], off offset:2048
	global_load_dwordx4 v[10:13], v[2:3], off offset:3072
	v_add_co_u32_e32 v2, vcc, s2, v2
	s_mul_i32 s14, s4, 0x1800
	s_nop 0
	v_addc_co_u32_e32 v3, vcc, 0, v3, vcc
	global_load_dwordx4 v[6:9], v[2:3], off
	s_nop 0
	global_load_dwordx4 v[2:5], v[2:3], off offset:1024
	s_barrier
	ds_read_b128 v[104:107], v40
	v_or_b32_e32 v40, 0x18800, v57
	ds_read_b128 v[136:139], v40
	v_or_b32_e32 v40, 0x19000, v57
	s_waitcnt vmcnt(17) lgkmcnt(1)
	v_mfma_f32_16x16x32_f16 v[24:27], v[64:67], v[104:107], v[24:27]
	v_lshl_add_u64 v[18:19], v[18:19], 0, s[14:15]
	s_lshl_b64 s[4:5], s[12:13], 7
	s_add_u32 s4, s10, s4
	s_waitcnt vmcnt(16)
	v_mfma_f32_16x16x32_f16 v[36:39], v[68:71], v[104:107], v[36:39]
	s_addc_u32 s5, s11, s5
	s_waitcnt vmcnt(15)
	v_mfma_f32_16x16x32_f16 v[76:79], v[104:107], v[116:119], v[76:79]
	ds_read_b128 v[104:107], v40
	v_or_b32_e32 v40, 0x19800, v57
	s_waitcnt lgkmcnt(1)
	v_mfma_f32_16x16x32_f16 v[28:31], v[64:67], v[136:139], v[28:31]
	v_mfma_f32_16x16x32_f16 v[84:87], v[68:71], v[136:139], v[84:87]
	v_mfma_f32_16x16x32_f16 v[20:23], v[136:139], v[116:119], v[20:23]
	ds_read_b128 v[136:139], v40
	v_or_b32_e32 v40, 0x18000, v58
	s_waitcnt lgkmcnt(1)
	v_mfma_f32_16x16x32_f16 v[72:75], v[68:71], v[104:107], v[72:75]
	s_waitcnt lgkmcnt(0)
	v_mfma_f32_16x16x32_f16 v[68:71], v[68:71], v[136:139], v[88:91]
	s_nop 2
	ds_read_b128 v[88:91], v40
	v_or_b32_e32 v40, 0x18800, v58
	v_mfma_f32_16x16x32_f16 v[60:63], v[64:67], v[104:107], v[60:63]
	v_mfma_f32_16x16x32_f16 v[64:67], v[64:67], v[136:139], v[80:83]
	v_mfma_f32_16x16x32_f16 v[80:83], v[136:139], v[116:119], v[92:95]
	s_nop 2
	ds_read_b128 v[92:95], v40
	v_mfma_f32_16x16x32_f16 v[32:35], v[104:107], v[116:119], v[32:35]
	s_waitcnt vmcnt(14) lgkmcnt(1)
	v_mfma_f32_16x16x32_f16 v[104:107], v[120:123], v[88:91], v[24:27]
	s_nop 2
	v_or_b32_e32 v24, 0x19000, v58
	s_waitcnt vmcnt(13)
	v_mfma_f32_16x16x32_f16 v[116:119], v[124:127], v[88:91], v[36:39]
	s_waitcnt vmcnt(12)
	v_mfma_f32_16x16x32_f16 v[76:79], v[88:91], v[128:131], v[76:79]
	s_waitcnt lgkmcnt(0)
	v_mfma_f32_16x16x32_f16 v[88:91], v[120:123], v[92:95], v[28:31]
	v_mfma_f32_16x16x32_f16 v[84:87], v[124:127], v[92:95], v[84:87]
	v_mfma_f32_16x16x32_f16 v[92:95], v[92:95], v[128:131], v[20:23]
	s_nop 2
	ds_read_b128 v[20:23], v24
	v_or_b32_e32 v24, 0x19800, v58
	ds_read_b128 v[24:27], v24
	s_waitcnt lgkmcnt(1)
	v_mfma_f32_16x16x32_f16 v[60:63], v[120:123], v[20:23], v[60:63]
	v_mfma_f32_16x16x32_f16 v[72:75], v[124:127], v[20:23], v[72:75]
	v_mfma_f32_16x16x32_f16 v[136:139], v[20:23], v[128:131], v[32:35]
	s_waitcnt lgkmcnt(0)
	v_mfma_f32_16x16x32_f16 v[64:67], v[120:123], v[24:27], v[64:67]
	v_mfma_f32_16x16x32_f16 v[68:71], v[124:127], v[24:27], v[68:71]
	v_mfma_f32_16x16x32_f16 v[80:83], v[24:27], v[128:131], v[80:83]
	global_load_dwordx4 v[38:41], v[18:19], off
	global_load_dwordx4 v[34:37], v[18:19], off offset:1024
	global_load_dwordx4 v[30:33], v[18:19], off offset:2048
	global_load_dwordx4 v[22:25], v[18:19], off offset:3072
	v_add_co_u32_e32 v18, vcc, s2, v18
	s_mov_b32 s2, 0x3c800000
	s_nop 0
	v_addc_co_u32_e32 v19, vcc, 0, v19, vcc
	global_load_dwordx4 v[26:29], v[18:19], off
	s_nop 0
	global_load_dwordx4 v[18:21], v[18:19], off offset:1024
	s_barrier
	ds_read_b128 v[120:123], v59
	v_or_b32_e32 v59, 0x1a800, v57
	ds_read_b128 v[124:127], v59
	v_or_b32_e32 v59, 0x1b000, v57
	s_waitcnt vmcnt(17) lgkmcnt(1)
	v_mfma_f32_16x16x32_f16 v[104:107], v[50:53], v[120:123], v[104:107]
	s_waitcnt vmcnt(16)
	v_mfma_f32_16x16x32_f16 v[116:119], v[96:99], v[120:123], v[116:119]
	s_waitcnt vmcnt(15)
	v_mfma_f32_16x16x32_f16 v[76:79], v[120:123], v[100:103], v[76:79]
	ds_read_b128 v[120:123], v59
	v_or_b32_e32 v59, 0x1b800, v57
	s_waitcnt lgkmcnt(1)
	v_mfma_f32_16x16x32_f16 v[88:91], v[50:53], v[124:127], v[88:91]
	v_mfma_f32_16x16x32_f16 v[84:87], v[96:99], v[124:127], v[84:87]
	v_mfma_f32_16x16x32_f16 v[92:95], v[124:127], v[100:103], v[92:95]
	ds_read_b128 v[124:127], v59
	v_or_b32_e32 v59, 0x1a000, v58
	s_waitcnt lgkmcnt(1)
	v_mfma_f32_16x16x32_f16 v[60:63], v[50:53], v[120:123], v[60:63]
	s_waitcnt lgkmcnt(0)
	v_mfma_f32_16x16x32_f16 v[50:53], v[50:53], v[124:127], v[64:67]
	v_mfma_f32_16x16x32_f16 v[64:67], v[96:99], v[124:127], v[68:71]
	v_mfma_f32_16x16x32_f16 v[68:71], v[124:127], v[100:103], v[80:83]
	v_or_b32_e32 v124, 0x1d800, v58
	s_nop 1
	ds_read_b128 v[80:83], v59
	v_or_b32_e32 v59, 0x1a800, v58
	v_mfma_f32_16x16x32_f16 v[72:75], v[96:99], v[120:123], v[72:75]
	ds_read_b128 v[96:99], v59
	v_or_b32_e32 v59, 0x1b000, v58
	v_mfma_f32_16x16x32_f16 v[120:123], v[120:123], v[100:103], v[136:139]
	s_waitcnt vmcnt(14) lgkmcnt(1)
	v_mfma_f32_16x16x32_f16 v[100:103], v[108:111], v[80:83], v[104:107]
	s_waitcnt vmcnt(13)
	v_mfma_f32_16x16x32_f16 v[104:107], v[112:115], v[80:83], v[116:119]
	s_waitcnt vmcnt(12)
	v_mfma_f32_16x16x32_f16 v[76:79], v[80:83], v[132:135], v[76:79]
	s_waitcnt lgkmcnt(0)
	v_mfma_f32_16x16x32_f16 v[80:83], v[108:111], v[96:99], v[88:91]
	v_mfma_f32_16x16x32_f16 v[88:91], v[96:99], v[132:135], v[92:95]
	s_nop 2
	ds_read_b128 v[92:95], v59
	v_or_b32_e32 v59, 0x1b800, v58
	v_mfma_f32_16x16x32_f16 v[84:87], v[112:115], v[96:99], v[84:87]
	ds_read_b128 v[96:99], v59
	v_or_b32_e32 v59, 0x1c000, v57
	s_waitcnt lgkmcnt(0)
	v_mfma_f32_16x16x32_f16 v[60:63], v[108:111], v[92:95], v[60:63]
	s_barrier
	v_mfma_f32_16x16x32_f16 v[108:111], v[108:111], v[96:99], v[50:53]
	v_mfma_f32_16x16x32_f16 v[50:53], v[96:99], v[132:135], v[68:71]
	s_nop 2
	ds_read_b128 v[68:71], v59
	v_or_b32_e32 v59, 0x1c800, v57
	v_mfma_f32_16x16x32_f16 v[64:67], v[112:115], v[96:99], v[64:67]
	ds_read_b128 v[96:99], v59
	v_or_b32_e32 v59, 0x1d000, v57
	v_mfma_f32_16x16x32_f16 v[72:75], v[112:115], v[92:95], v[72:75]
	v_or_b32_e32 v112, 0x1d800, v57
	v_mfma_f32_16x16x32_f16 v[92:95], v[92:95], v[132:135], v[120:123]
	v_or_b32_e32 v132, 0x1e800, v57
	s_waitcnt vmcnt(11) lgkmcnt(1)
	v_mfma_f32_16x16x32_f16 v[100:103], v[46:49], v[68:71], v[100:103]
	v_or_b32_e32 v120, 0x1c800, v58
	s_waitcnt vmcnt(10)
	v_mfma_f32_16x16x32_f16 v[104:107], v[42:45], v[68:71], v[104:107]
	s_waitcnt vmcnt(9)
	v_mfma_f32_16x16x32_f16 v[68:71], v[68:71], v[14:17], v[76:79]
	s_waitcnt lgkmcnt(0)
	v_mfma_f32_16x16x32_f16 v[76:79], v[46:49], v[96:99], v[80:83]
	s_nop 2
	ds_read_b128 v[80:83], v59
	ds_read_b128 v[112:115], v112
	v_or_b32_e32 v59, 0x1c000, v58
	ds_read_b128 v[116:119], v59
	ds_read_b128 v[120:123], v120
	v_or_b32_e32 v59, 0x1d000, v58
	v_mfma_f32_16x16x32_f16 v[84:87], v[42:45], v[96:99], v[84:87]
	v_mfma_f32_16x16x32_f16 v[88:91], v[96:99], v[14:17], v[88:91]
	ds_read_b128 v[96:99], v59
	ds_read_b128 v[124:127], v124
	v_or_b32_e32 v59, 0x1e000, v57
	s_waitcnt lgkmcnt(0)
	s_barrier
	s_waitcnt vmcnt(8)
	v_mfma_f32_16x16x32_f16 v[100:103], v[10:13], v[116:119], v[100:103]
	ds_read_b128 v[128:131], v59
	ds_read_b128 v[132:135], v132
	v_or_b32_e32 v59, 0x1f000, v57
	v_or_b32_e32 v57, 0x1f800, v57
	s_waitcnt vmcnt(7)
	v_mfma_f32_16x16x32_f16 v[104:107], v[6:9], v[116:119], v[104:107]
	ds_read_b128 v[136:139], v59
	ds_read_b128 v[140:143], v57
	v_or_b32_e32 v57, 0x1e000, v58
	v_or_b32_e32 v59, 0x1e800, v58
	s_waitcnt vmcnt(6)
	v_mfma_f32_16x16x32_f16 v[68:71], v[116:119], v[2:5], v[68:71]
	ds_read_b128 v[116:119], v57
	ds_read_b128 v[144:147], v59
	v_or_b32_e32 v57, 0x1f000, v58
	v_or_b32_e32 v58, 0x1f800, v58
	s_waitcnt vmcnt(5) lgkmcnt(5)
	v_mfma_f32_16x16x32_f16 v[100:103], v[38:41], v[128:131], v[100:103]
	ds_read_b128 v[148:151], v57
	ds_read_b128 v[152:155], v58
	v_lshl_add_u64 v[58:59], s[4:5], 0, v[54:55]
	v_and_b32_e32 v54, 48, v0
	s_waitcnt vmcnt(4)
	v_mfma_f32_16x16x32_f16 v[104:107], v[34:37], v[128:131], v[104:107]
	s_lshl_b32 s4, s16, 5
	s_waitcnt vmcnt(3)
	v_mfma_f32_16x16x32_f16 v[68:71], v[128:131], v[30:33], v[68:71]
	v_lshl_add_u64 v[128:129], v[58:59], 0, v[54:55]
	s_waitcnt vmcnt(2) lgkmcnt(3)
	v_mfma_f32_16x16x32_f16 v[100:103], v[22:25], v[116:119], v[100:103]
	s_waitcnt vmcnt(1)
	v_mfma_f32_16x16x32_f16 v[104:107], v[26:29], v[116:119], v[104:107]
	s_waitcnt vmcnt(0)
	v_mfma_f32_16x16x32_f16 v[68:71], v[116:119], v[18:21], v[68:71]
	s_nop 3
	v_mov_b32_e32 v54, v101
	v_mov_b32_e32 v55, v102
	v_pk_mul_f32 v[54:55], v[54:55], s[2:3] op_sel_hi:[1,0]
	v_mfma_f32_16x16x32_f16 v[76:79], v[10:13], v[120:123], v[76:79]
	v_fma_mixlo_f16 v57, v100, s2, 0
	v_cvt_pk_f16_f32 v100, v54, v55
	v_mov_b32_e32 v54, v105
	v_mov_b32_e32 v55, v106
	v_mfma_f32_16x16x32_f16 v[84:87], v[6:9], v[120:123], v[84:87]
	v_mul_f32_e64 v54, v54, s2
	v_mul_f32_e64 v55, v55, s2
	v_pack_b32_f16 v58, v57, v100
	v_cvt_pk_f16_f32 v57, v54, v55
	v_mov_b32_e32 v54, v69
	v_mfma_f32_16x16x32_f16 v[88:91], v[120:123], v[2:5], v[88:91]
	v_mov_b32_e32 v55, v70
	v_pk_mul_f32 v[54:55], v[54:55], s[2:3] op_sel_hi:[1,0]
	v_fma_mixlo_f16 v59, v104, s2, 0
	v_mfma_f32_16x16x32_f16 v[76:79], v[38:41], v[132:135], v[76:79]
	v_cvt_pk_f16_f32 v70, v54, v55
	v_fma_mixlo_f16 v54, v103, s2, 0
	v_fma_mixlo_f16 v104, v68, s2, 0
	v_mfma_f32_16x16x32_f16 v[84:87], v[34:37], v[132:135], v[84:87]
	v_pack_b32_f16 v68, v59, v57
	v_alignbit_b32 v59, v54, v100, 16
	v_fma_mixlo_f16 v54, v107, s2, 0
	v_alignbit_b32 v69, v54, v57, 16
	v_lshlrev_b64 v[100:101], 7, v[156:157]
	v_mfma_f32_16x16x32_f16 v[88:91], v[132:135], v[30:33], v[88:91]
	v_lshl_or_b32 v105, v56, 3, s4
	v_or_b32_e32 v100, v100, v105
	v_lshl_add_u64 v[102:103], s[6:7], 0, v[100:101]
	s_waitcnt lgkmcnt(2)
	v_mfma_f32_16x16x32_f16 v[54:57], v[22:25], v[144:147], v[76:79]
	global_store_dwordx2 v[102:103], v[58:59], off sc1
	v_lshl_add_u64 v[58:59], s[8:9], 0, v[100:101]
	global_store_dwordx2 v[58:59], v[68:69], off sc1
	v_mfma_f32_16x16x32_f16 v[76:79], v[26:29], v[144:147], v[84:87]
	v_or_b32_e32 v68, 16, v156
	s_nop 2
	v_fma_mixlo_f16 v58, v54, s2, 0
	v_mov_b32_e32 v54, v55
	v_mfma_f32_16x16x32_f16 v[84:87], v[144:147], v[18:21], v[88:91]
	v_mov_b32_e32 v55, v56
	v_pk_mul_f32 v[54:55], v[54:55], s[2:3] op_sel_hi:[1,0]
	v_fma_mixlo_f16 v59, v76, s2, 0
	v_mfma_f32_16x16x32_f16 v[60:63], v[46:49], v[80:83], v[60:63]
	v_cvt_pk_f16_f32 v56, v54, v55
	v_mov_b32_e32 v54, v77
	v_mov_b32_e32 v55, v78
	v_mfma_f32_16x16x32_f16 v[72:75], v[42:45], v[80:83], v[72:75]
	v_mul_f32_e64 v54, v54, s2
	v_mul_f32_e64 v55, v55, s2
	v_pack_b32_f16 v76, v58, v56
	v_ashrrev_i32_e32 v69, 31, v68
	v_mfma_f32_16x16x32_f16 v[80:83], v[80:83], v[14:17], v[92:95]
	v_lshlrev_b64 v[68:69], 7, v[68:69]
	v_or_b32_e32 v68, v68, v105
	v_fma_mixlo_f16 v84, v84, s2, 0
	v_mfma_f32_16x16x32_f16 v[42:45], v[42:45], v[112:115], v[64:67]
	s_nop 2
	v_cvt_pk_f16_f32 v67, v54, v55
	v_mov_b32_e32 v54, v85
	v_mov_b32_e32 v55, v86
	v_pk_mul_f32 v[54:55], v[54:55], s[2:3] op_sel_hi:[1,0]
	v_pack_b32_f16 v66, v59, v67
	v_mfma_f32_16x16x32_f16 v[58:61], v[10:13], v[96:99], v[60:63]
	v_mfma_f32_16x16x32_f16 v[62:65], v[6:9], v[96:99], v[72:75]
	s_nop 2
	v_cvt_pk_f16_f32 v74, v54, v55
	v_fma_mixlo_f16 v54, v57, s2, 0
	v_alignbit_b32 v77, v54, v56, 16
	v_mfma_f32_16x16x32_f16 v[54:57], v[96:99], v[2:5], v[80:83]
	v_fma_mixlo_f16 v72, v79, s2, 0
	v_alignbit_b32 v67, v72, v67, 16
	v_lshl_add_u64 v[72:73], s[6:7], 0, v[68:69]
	v_mfma_f32_16x16x32_f16 v[46:49], v[46:49], v[112:115], v[108:111]
	v_lshl_add_u64 v[68:69], s[8:9], 0, v[68:69]
	global_store_dwordx2 v[68:69], v[66:67], off sc1
	v_lshrrev_b32_e32 v67, 16, v70
	v_mfma_f32_16x16x32_f16 v[58:61], v[38:41], v[136:139], v[58:61]
	v_lshrrev_b32_e32 v69, 16, v74
	v_fma_mixhi_f16 v69, v87, s2, 0
	v_fma_mixhi_f16 v67, v71, s2, 0
	v_mfma_f32_16x16x32_f16 v[54:57], v[136:139], v[30:33], v[54:57]
	v_pack_b32_f16 v68, v84, v74
	v_pack_b32_f16 v66, v104, v70
	global_store_dwordx4 v[128:129], v[66:69], off sc1
	v_mfma_f32_16x16x32_f16 v[62:65], v[34:37], v[136:139], v[62:65]
	global_store_dwordx2 v[72:73], v[76:77], off sc1
	v_or_b32_e32 v66, 32, v156
	v_ashrrev_i32_e32 v67, 31, v66
	v_mfma_f32_16x16x32_f16 v[14:17], v[112:115], v[14:17], v[50:53]
	v_mfma_f32_16x16x32_f16 v[6:9], v[6:9], v[124:127], v[42:45]
	s_waitcnt lgkmcnt(1)
	v_mfma_f32_16x16x32_f16 v[58:61], v[22:25], v[148:151], v[58:61]
	v_mfma_f32_16x16x32_f16 v[54:57], v[148:151], v[18:21], v[54:57]
	v_mfma_f32_16x16x32_f16 v[10:13], v[10:13], v[124:127], v[46:49]
	s_nop 5
	v_fma_mixlo_f16 v68, v58, s2, 0
	v_mov_b32_e32 v58, v59
	v_mov_b32_e32 v59, v60
	v_mfma_f32_16x16x32_f16 v[62:65], v[26:29], v[148:151], v[62:65]
	v_mul_f32_e64 v50, v58, s2
	v_mul_f32_e64 v51, v59, s2
	v_fma_mixlo_f16 v54, v54, s2, 0
	v_cvt_pk_f16_f32 v50, v50, v51
	v_mfma_f32_16x16x32_f16 v[2:5], v[124:127], v[2:5], v[14:17]
	v_pack_b32_f16 v46, v68, v50
	s_nop 1
	v_mov_b32_e32 v48, v63
	v_mov_b32_e32 v49, v64
	v_mfma_f32_16x16x32_f16 v[6:9], v[34:37], v[140:143], v[6:9]
	v_mov_b32_e32 v14, v55
	v_mov_b32_e32 v15, v56
	v_pk_mul_f32 v[14:15], v[14:15], s[2:3] op_sel_hi:[1,0]
	v_mfma_f32_16x16x32_f16 v[10:13], v[38:41], v[140:143], v[10:13]
	v_mul_f32_e64 v42, v48, s2
	v_mul_f32_e64 v43, v49, s2
	v_cvt_pk_f16_f32 v38, v14, v15
	v_fma_mixlo_f16 v14, v61, s2, 0
	v_mfma_f32_16x16x32_f16 v[2:5], v[140:143], v[30:33], v[2:5]
	v_fma_mixlo_f16 v62, v62, s2, 0
	v_cvt_pk_f16_f32 v43, v42, v43
	v_alignbit_b32 v47, v14, v50, 16
	v_fma_mixlo_f16 v14, v65, s2, 0
	s_waitcnt lgkmcnt(0)
	v_mfma_f32_16x16x32_f16 v[6:9], v[26:29], v[152:155], v[6:9]
	v_pack_b32_f16 v42, v62, v43
	v_alignbit_b32 v43, v14, v43, 16
	v_lshlrev_b64 v[14:15], 7, v[66:67]
	v_mfma_f32_16x16x32_f16 v[10:13], v[22:25], v[152:155], v[10:13]
	v_or_b32_e32 v14, v14, v105
	v_lshl_add_u64 v[16:17], s[6:7], 0, v[14:15]
	global_store_dwordx2 v[16:17], v[46:47], off sc1
	v_mfma_f32_16x16x32_f16 v[2:5], v[152:155], v[18:21], v[2:5]
	v_lshl_add_u64 v[14:15], s[8:9], 0, v[14:15]
	v_fma_mixlo_f16 v17, v6, s2, 0
	v_mov_b32_e32 v6, v7
	v_mov_b32_e32 v7, v8
	global_store_dwordx2 v[14:15], v[42:43], off sc1
	v_or_b32_e32 v14, 48, v156
	v_fma_mixlo_f16 v16, v10, s2, 0
	v_mov_b32_e32 v10, v11
	v_mov_b32_e32 v11, v12
	v_pk_mul_f32 v[6:7], v[6:7], s[2:3] op_sel_hi:[1,0]
	v_ashrrev_i32_e32 v15, 31, v14
	v_pk_mul_f32 v[10:11], v[10:11], s[2:3] op_sel_hi:[1,0]
	v_cvt_pk_f16_f32 v7, v6, v7
	v_fma_mixlo_f16 v8, v9, s2, 0
	v_cvt_pk_f16_f32 v12, v10, v11
	v_pack_b32_f16 v6, v17, v7
	v_mov_b32_e32 v10, v3
	v_mov_b32_e32 v11, v4
	v_alignbit_b32 v7, v8, v7, 16
	v_lshlrev_b64 v[8:9], 7, v[14:15]
	v_pk_mul_f32 v[10:11], v[10:11], s[2:3] op_sel_hi:[1,0]
	v_fma_mixlo_f16 v3, v13, s2, 0
	v_or_b32_e32 v8, v8, v105
	v_fma_mixlo_f16 v18, v2, s2, 0
	v_pack_b32_f16 v2, v16, v12
	v_cvt_pk_f16_f32 v4, v10, v11
	v_alignbit_b32 v3, v3, v12, 16
	v_lshl_add_u64 v[10:11], s[6:7], 0, v[8:9]
	global_store_dwordx2 v[10:11], v[2:3], off sc1
	v_lshl_add_u64 v[2:3], s[8:9], 0, v[8:9]
	global_store_dwordx2 v[2:3], v[6:7], off sc1
	v_lshrrev_b32_e32 v7, 16, v38
	v_lshrrev_b32_e32 v9, 16, v4
	v_fma_mixhi_f16 v9, v5, s2, 0
	v_fma_mixhi_f16 v7, v57, s2, 0
	v_pack_b32_f16 v8, v18, v4
	v_pack_b32_f16 v6, v54, v38
	global_store_dwordx4 v[128:129], v[6:9], off offset:64 sc1
	s_cbranch_execnz .LBB1_2

.LBB3_20:
	s_mov_b32 s4, 0xf149f2ca
	s_waitcnt vmcnt(0)
	v_max3_f32 v7, v8, s4, v36
	v_max3_f32 v7, v7, v0, v18
	v_max3_f32 v7, v7, v14, v30
	v_max3_f32 v15, v7, v26, v34
	v_sub_f32_e32 v7, v8, v15
	v_exp_f32_e32 v40, v7
	v_sub_f32_e32 v7, v36, v15
	v_exp_f32_e32 v41, v7
	v_cvt_f32_f16_sdwa v43, v4 dst_sel:DWORD dst_unused:UNUSED_PAD src0_sel:WORD_1
	v_cvt_f32_f16_sdwa v45, v5 dst_sel:DWORD dst_unused:UNUSED_PAD src0_sel:WORD_1
	v_cvt_f32_f16_e32 v44, v5
	v_cvt_f32_f16_e32 v42, v4
	v_mov_b32_e32 v7, v37
	v_pk_mul_f32 v[4:5], v[6:7], v[40:41]
	v_cvt_f32_f16_sdwa v37, v10 dst_sel:DWORD dst_unused:UNUSED_PAD src0_sel:WORD_1
	v_cvt_f32_f16_e32 v36, v10
	v_cvt_f32_f16_sdwa v41, v11 dst_sel:DWORD dst_unused:UNUSED_PAD src0_sel:WORD_1
	v_cvt_f32_f16_e32 v40, v11
	v_pk_fma_f32 v[6:7], v[44:45], v[4:5], 0 op_sel_hi:[1,0,0]
	v_pk_fma_f32 v[10:11], v[42:43], v[4:5], 0 op_sel_hi:[1,0,0]
	v_sub_f32_e32 v0, v0, v15
	v_add_f32_e32 v8, 0, v4
	v_pk_fma_f32 v[10:11], v[36:37], v[4:5], v[10:11] op_sel:[0,1,0]
	v_pk_fma_f32 v[6:7], v[40:41], v[4:5], v[6:7] op_sel:[0,1,0]
	v_exp_f32_e32 v4, v0
	v_sub_f32_e32 v0, v18, v15
	v_add_f32_e32 v8, v8, v5
	v_exp_f32_e32 v5, v0
	v_cvt_f32_f16_sdwa v41, v3 dst_sel:DWORD dst_unused:UNUSED_PAD src0_sel:WORD_1
	v_cvt_f32_f16_e32 v40, v3
	v_mov_b32_e32 v18, v1
	v_cvt_f32_f16_sdwa v37, v2 dst_sel:DWORD dst_unused:UNUSED_PAD src0_sel:WORD_1
	v_cvt_f32_f16_e32 v36, v2
	v_pk_mul_f32 v[0:1], v[18:19], v[4:5]
	v_cvt_f32_f16_sdwa v5, v16 dst_sel:DWORD dst_unused:UNUSED_PAD src0_sel:WORD_1
	v_pk_fma_f32 v[2:3], v[40:41], v[0:1], v[6:7] op_sel_hi:[1,0,1]
	v_cvt_f32_f16_e32 v4, v16
	v_cvt_f32_f16_sdwa v7, v17 dst_sel:DWORD dst_unused:UNUSED_PAD src0_sel:WORD_1
	v_cvt_f32_f16_e32 v6, v17
	v_pk_fma_f32 v[10:11], v[36:37], v[0:1], v[10:11] op_sel_hi:[1,0,1]
	v_add_f32_e32 v8, v8, v0
	v_pk_fma_f32 v[4:5], v[4:5], v[0:1], v[10:11] op_sel:[0,1,0]
	v_pk_fma_f32 v[2:3], v[6:7], v[0:1], v[2:3] op_sel:[0,1,0]
	v_add_f32_e32 v8, v8, v1
	v_sub_f32_e32 v0, v14, v15
	v_sub_f32_e32 v1, v30, v15
	v_exp_f32_e32 v0, v0
	v_exp_f32_e32 v1, v1
	v_cvt_f32_f16_sdwa v7, v23 dst_sel:DWORD dst_unused:UNUSED_PAD src0_sel:WORD_1
	v_cvt_f32_f16_e32 v6, v23
	v_cvt_f32_f16_sdwa v11, v22 dst_sel:DWORD dst_unused:UNUSED_PAD src0_sel:WORD_1
	v_cvt_f32_f16_e32 v10, v22
	v_pk_mul_f32 v[0:1], v[12:13], v[0:1]
	v_cvt_f32_f16_sdwa v13, v29 dst_sel:DWORD dst_unused:UNUSED_PAD src0_sel:WORD_1
	v_pk_fma_f32 v[2:3], v[6:7], v[0:1], v[2:3] op_sel_hi:[1,0,1]
	v_cvt_f32_f16_sdwa v7, v28 dst_sel:DWORD dst_unused:UNUSED_PAD src0_sel:WORD_1
	v_cvt_f32_f16_e32 v6, v28
	v_cvt_f32_f16_e32 v12, v29
	v_pk_fma_f32 v[4:5], v[10:11], v[0:1], v[4:5] op_sel_hi:[1,0,1]
	v_add_f32_e32 v8, v8, v0
	v_pk_fma_f32 v[4:5], v[6:7], v[0:1], v[4:5] op_sel:[0,1,0]
	v_pk_fma_f32 v[2:3], v[12:13], v[0:1], v[2:3] op_sel:[0,1,0]
	v_add_f32_e32 v8, v8, v1
	v_sub_f32_e32 v0, v26, v15
	v_sub_f32_e32 v1, v34, v15
	v_exp_f32_e32 v0, v0
	v_exp_f32_e32 v1, v1
	v_cvt_f32_f16_sdwa v7, v33 dst_sel:DWORD dst_unused:UNUSED_PAD src0_sel:WORD_1
	v_cvt_f32_f16_e32 v6, v33
	v_cvt_f32_f16_sdwa v11, v32 dst_sel:DWORD dst_unused:UNUSED_PAD src0_sel:WORD_1
	v_pk_mul_f32 v[0:1], v[24:25], v[0:1]
	v_cvt_f32_f16_e32 v10, v32
	v_add_f32_e32 v8, v8, v0
	v_add_f32_e32 v8, v8, v1
	v_div_scale_f32 v14, s[4:5], v8, v8, 1.0
	v_pk_fma_f32 v[2:3], v[6:7], v[0:1], v[2:3] op_sel_hi:[1,0,1]
	v_cvt_f32_f16_sdwa v7, v20 dst_sel:DWORD dst_unused:UNUSED_PAD src0_sel:WORD_1
	v_cvt_f32_f16_e32 v6, v20
	v_cvt_f32_f16_sdwa v13, v21 dst_sel:DWORD dst_unused:UNUSED_PAD src0_sel:WORD_1
	v_cvt_f32_f16_e32 v12, v21
	v_rcp_f32_e32 v15, v14
	v_pk_fma_f32 v[4:5], v[10:11], v[0:1], v[4:5] op_sel_hi:[1,0,1]
	s_add_i32 s0, s8, 3
	v_pk_fma_f32 v[4:5], v[6:7], v[0:1], v[4:5] op_sel:[0,1,0]
	v_pk_fma_f32 v[0:1], v[12:13], v[0:1], v[2:3] op_sel:[0,1,0]
	v_fma_f32 v2, -v14, v15, 1.0
	v_fmac_f32_e32 v15, v2, v15
	v_div_scale_f32 v2, vcc, 1.0, v8, 1.0
	v_mul_f32_e32 v3, v2, v15
	v_fma_f32 v6, -v14, v3, v2
	v_fmac_f32_e32 v3, v6, v15
	v_fma_f32 v2, -v14, v3, v2
	s_lshl_b64 s[0:1], s[0:1], 15
	v_div_fmas_f32 v2, v2, v15, v3
	s_add_u32 s0, s2, s0
	v_div_fixup_f32 v6, v2, v8, 1.0
	s_addc_u32 s1, s3, s1
	v_lshlrev_b32_e32 v8, 8, v38
	v_pk_mul_f32 v[2:3], v[0:1], v[6:7] op_sel_hi:[1,0]
	v_pk_mul_f32 v[0:1], v[4:5], v[6:7] op_sel_hi:[1,0]
	v_lshl_add_u64 v[4:5], s[0:1], 0, v[8:9]
	v_lshlrev_b32_e32 v8, 2, v39
	v_lshl_add_u64 v[4:5], v[4:5], 0, v[8:9]
	global_store_dwordx4 v[4:5], v[0:3], off sc1
